# DIFF + MoBA attention: QK K-fragment reads prefetched into distinct dead VGPR quads with counted lgkmcnt waits
# baseline (speedup 1.0000x reference)
.LBB0_969:
	v_mov_b32_e32 v66, 0xff800000
	s_and_saveexec_b64 s[44:45], s[34:35]
	v_xor_b32_e32 v66, 0x80000000, v146
	s_or_b64 exec, exec, s[44:45]
	s_lshl_b32 s34, s65, 14
	v_add_u32_e32 v115, s34, v134
	ds_read_b128 v[116:119], v115
	v_mov_b32_e32 v67, v66
	v_mov_b32_e32 v68, v66
	v_mov_b32_e32 v69, v66
	v_mov_b32_e32 v70, v66
	v_mov_b32_e32 v71, v66
	v_mov_b32_e32 v72, v66
	v_mov_b32_e32 v73, v66
	v_mov_b32_e32 v74, v66
	v_mov_b32_e32 v75, v66
	v_mov_b32_e32 v76, v66
	v_mov_b32_e32 v77, v66
	v_mov_b32_e32 v78, v66
	v_mov_b32_e32 v79, v66
	v_mov_b32_e32 v80, v66
	v_mov_b32_e32 v81, v66
	ds_read_b128 v[120:123], v115 offset:4096
	v_add_u32_e32 v115, s34, v135
	ds_read_b128 v[124:127], v115
	ds_read_b128 v[148:151], v115 offset:4096
	v_add_u32_e32 v115, s34, v136
	ds_read_b128 v[152:155], v115
	ds_read_b128 v[156:159], v115 offset:4096
	v_add_u32_e32 v115, s34, v137
	ds_read_b128 v[164:167], v115
	ds_read_b128 v[168:171], v115 offset:4096
	s_waitcnt lgkmcnt(7)
	s_nop 0
	v_mfma_f32_32x32x16_f16 v[82:97], v[116:119], v[98:101], v[66:81]
	s_waitcnt lgkmcnt(6)
	v_mfma_f32_32x32x16_f16 v[66:81], v[120:123], v[98:101], v[66:81]
	s_waitcnt lgkmcnt(5)
	v_mfma_f32_32x32x16_f16 v[82:97], v[124:127], v[102:105], v[82:97]
	s_waitcnt lgkmcnt(4)
	v_mfma_f32_32x32x16_f16 v[66:81], v[148:151], v[102:105], v[66:81]
	s_waitcnt lgkmcnt(3)
	v_mfma_f32_32x32x16_f16 v[82:97], v[152:155], v[106:109], v[82:97]
	s_waitcnt lgkmcnt(2)
	v_mfma_f32_32x32x16_f16 v[66:81], v[156:159], v[106:109], v[66:81]
	s_waitcnt lgkmcnt(1)
	v_mfma_f32_32x32x16_f16 v[82:97], v[164:167], v[110:113], v[82:97]
	s_waitcnt lgkmcnt(0)
	v_mfma_f32_32x32x16_f16 v[66:81], v[168:171], v[110:113], v[66:81]

.LBB0_993:
	v_mov_b32_e32 v2, 0xff800000
	s_and_saveexec_b64 s[42:43], s[34:35]
	v_xor_b32_e32 v2, 0x80000000, v146
	s_or_b64 exec, exec, s[42:43]
	s_lshl_b32 s34, s44, 14
	v_add_u32_e32 v115, s34, v134
	ds_read_b128 v[116:119], v115
	v_mov_b32_e32 v3, v2
	v_mov_b32_e32 v4, v2
	v_mov_b32_e32 v5, v2
	v_mov_b32_e32 v6, v2
	v_mov_b32_e32 v7, v2
	v_mov_b32_e32 v8, v2
	v_mov_b32_e32 v9, v2
	v_mov_b32_e32 v10, v2
	v_mov_b32_e32 v11, v2
	v_mov_b32_e32 v12, v2
	v_mov_b32_e32 v13, v2
	v_mov_b32_e32 v14, v2
	v_mov_b32_e32 v15, v2
	v_mov_b32_e32 v16, v2
	v_mov_b32_e32 v17, v2
	ds_read_b128 v[120:123], v115 offset:4096
	v_add_u32_e32 v115, s34, v135
	ds_read_b128 v[124:127], v115
	ds_read_b128 v[148:151], v115 offset:4096
	v_add_u32_e32 v115, s34, v136
	ds_read_b128 v[152:155], v115
	ds_read_b128 v[156:159], v115 offset:4096
	v_add_u32_e32 v115, s34, v137
	ds_read_b128 v[164:167], v115
	ds_read_b128 v[168:171], v115 offset:4096
	s_waitcnt lgkmcnt(7)
	s_nop 0
	v_mfma_f32_32x32x16_f16 v[18:33], v[116:119], v[98:101], v[2:17]
	s_waitcnt lgkmcnt(6)
	v_mfma_f32_32x32x16_f16 v[2:17], v[120:123], v[98:101], v[2:17]
	s_waitcnt lgkmcnt(5)
	v_mfma_f32_32x32x16_f16 v[18:33], v[124:127], v[102:105], v[18:33]
	s_waitcnt lgkmcnt(4)
	v_mfma_f32_32x32x16_f16 v[2:17], v[148:151], v[102:105], v[2:17]
	s_waitcnt lgkmcnt(3)
	v_mfma_f32_32x32x16_f16 v[18:33], v[152:155], v[106:109], v[18:33]
	s_waitcnt lgkmcnt(2)
	v_mfma_f32_32x32x16_f16 v[2:17], v[156:159], v[106:109], v[2:17]
	s_waitcnt lgkmcnt(1)
	v_mfma_f32_32x32x16_f16 v[18:33], v[164:167], v[110:113], v[18:33]
	s_waitcnt lgkmcnt(0)
	v_mfma_f32_32x32x16_f16 v[2:17], v[168:171], v[110:113], v[2:17]
